# P18 output stores tagged nt
# speedup vs baseline: 1.0037x; 1.0037x over previous
; __global__ void __launch_bounds__(NTHREADS, 2) fwd(Args args) {
;     ...
;         const bf16_t* X3 = (const bf16_t*)(ws + WS_R1); const f32x4* gr = (const f32x4*)args.in[22] + F.lane;
;         f32x4 gv[16];
; #pragma unroll
;         for (int j = 0; j < 16; ++j) gv[j] = gr[64 * j];
;         for (int m = F.bid * NWAVES + F.wave; m < T; m += F.G * NWAVES) { const u32x2* xr = (const u32x2*)(X3 + (size_t)m * D) + F.lane; f32x4 v[16]; float ss = 0.f;
; #pragma unroll
;             for (int j = 0; j < 16; ++j) { const u32x2 q = xr[64 * j]; v[j] = (f32x4){bflo(q.x), bfhi(q.x), bflo(q.y), bfhi(q.y)}; ss += (v[j].x * v[j].x + v[j].y * v[j].y) + (v[j].z * v[j].z + v[j].w * v[j].w); }
.LBB0_1794:
	global_load_dwordx2 v[68:69], v[64:65], off
	global_load_dwordx2 v[70:71], v[64:65], off offset:512
	global_load_dwordx2 v[72:73], v[64:65], off offset:1024
	global_load_dwordx2 v[74:75], v[64:65], off offset:1536
	global_load_dwordx2 v[76:77], v[64:65], off offset:2048
	global_load_dwordx2 v[78:79], v[64:65], off offset:2560
	global_load_dwordx2 v[80:81], v[64:65], off offset:3072
	global_load_dwordx2 v[82:83], v[64:65], off offset:3584
	v_add_co_u32_e32 v88, vcc, s10, v64
	s_add_i32 s2, s2, s4
	s_nop 0
	v_addc_co_u32_e32 v89, vcc, 0, v65, vcc
	global_load_dwordx2 v[100:101], v[88:89], off
	global_load_dwordx2 v[102:103], v[88:89], off offset:512
	global_load_dwordx2 v[104:105], v[88:89], off offset:1024
	global_load_dwordx2 v[106:107], v[88:89], off offset:1536
	global_load_dwordx2 v[108:109], v[88:89], off offset:2048
	global_load_dwordx2 v[110:111], v[88:89], off offset:2560
	global_load_dwordx2 v[112:113], v[88:89], off offset:3072
	global_load_dwordx2 v[114:115], v[88:89], off offset:3584
	v_add_co_u32_e32 v84, vcc, s10, v66
	v_lshl_add_u64 v[64:65], v[64:65], 0, s[8:9]
	s_nop 0
	v_addc_co_u32_e32 v85, vcc, 0, v67, vcc
	v_add_co_u32_e32 v86, vcc, s11, v66
	s_cmpk_lt_i32 s2, 0x2000
	s_nop 0
	v_addc_co_u32_e32 v87, vcc, 0, v67, vcc
	v_add_co_u32_e32 v90, vcc, s12, v66
	s_waitcnt vmcnt(15)
	v_lshlrev_b32_e32 v88, 16, v68
	v_and_b32_e32 v89, 0xffff0000, v68
	v_lshlrev_b32_e32 v68, 16, v69
	v_and_b32_e32 v69, 0xffff0000, v69
	s_waitcnt vmcnt(14)
	v_lshlrev_b32_e32 v117, 16, v71
	v_lshlrev_b32_e32 v116, 16, v70
	v_and_b32_e32 v71, 0xffff0000, v71
	v_and_b32_e32 v70, 0xffff0000, v70
	s_waitcnt vmcnt(13)
	v_and_b32_e32 v119, 0xffff0000, v72
	s_waitcnt vmcnt(12)
	v_lshlrev_b32_e32 v121, 16, v74
	s_waitcnt vmcnt(8)
	v_lshlrev_b32_e32 v131, 16, v82
	v_mul_f32_e32 v120, v69, v69
	v_pk_mul_f32 v[134:135], v[70:71], v[70:71]
	v_mul_f32_e32 v130, v89, v89
	v_lshlrev_b32_e32 v118, 16, v72
	v_lshlrev_b32_e32 v72, 16, v73
	v_and_b32_e32 v73, 0xffff0000, v73
	v_mov_b32_e32 v137, v121
	v_mul_f32_e32 v136, v119, v119
	v_mov_b32_e32 v164, v116
	v_mov_b32_e32 v165, v70
	v_mov_b32_e32 v70, v117
	v_pk_fma_f32 v[170:171], v[68:69], v[68:69], v[120:121] op_sel_hi:[1,1,0]
	v_pk_fma_f32 v[116:117], v[116:117], v[116:117], v[134:135]
	v_pk_fma_f32 v[134:135], v[88:89], v[88:89], v[130:131] op_sel_hi:[1,1,0]
	v_and_b32_e32 v123, 0xffff0000, v74
	v_lshlrev_b32_e32 v74, 16, v75
	v_and_b32_e32 v75, 0xffff0000, v75
	v_mul_f32_e32 v138, v73, v73
	v_mov_b32_e32 v139, v131
	v_pk_fma_f32 v[172:173], v[118:119], v[118:119], v[136:137] op_sel_hi:[1,1,0]
	v_mov_b32_e32 v120, v134
	v_mov_b32_e32 v136, v170
	v_mul_f32_e32 v180, v123, v123
	v_mul_f32_e32 v186, v74, v74
	v_mul_f32_e32 v196, v75, v75
	v_mov_b32_e32 v122, v121
	v_pk_fma_f32 v[174:175], v[72:73], v[72:73], v[138:139] op_sel_hi:[1,1,0]
	v_pk_add_f32 v[134:135], v[134:135], v[170:171]
	v_pk_add_f32 v[116:117], v[116:117], v[116:117] op_sel:[0,1] op_sel_hi:[1,0]
	v_pk_mul_f32 v[120:121], v[120:121], v[136:137]
	v_lshlrev_b32_e32 v125, 16, v77
	v_lshlrev_b32_e32 v124, 16, v76
	v_and_b32_e32 v77, 0xffff0000, v77
	v_and_b32_e32 v76, 0xffff0000, v76
	v_mov_b32_e32 v173, v186
	v_mov_b32_e32 v175, v196
	v_mov_b32_e32 v117, v180
	v_mov_b32_e32 v135, v121
	v_pk_mul_f32 v[140:141], v[76:77], v[76:77]
	v_pk_add_f32 v[136:137], v[172:173], v[174:175]
	v_pk_add_f32 v[116:117], v[134:135], v[116:117]
	v_lshlrev_b32_e32 v127, 16, v79
	v_lshlrev_b32_e32 v126, 16, v78
	v_and_b32_e32 v79, 0xffff0000, v79
	v_and_b32_e32 v78, 0xffff0000, v78
	s_waitcnt vmcnt(7)
	v_lshlrev_b32_e32 v149, 16, v101
	v_lshlrev_b32_e32 v148, 16, v100
	v_and_b32_e32 v101, 0xffff0000, v101
	v_and_b32_e32 v100, 0xffff0000, v100
	s_waitcnt vmcnt(5)
	v_lshlrev_b32_e32 v152, 16, v104
	v_and_b32_e32 v153, 0xffff0000, v104
	v_lshlrev_b32_e32 v104, 16, v105
	v_and_b32_e32 v105, 0xffff0000, v105
	v_mov_b32_e32 v166, v124
	v_mov_b32_e32 v167, v76
	v_mov_b32_e32 v76, v125
	v_pk_fma_f32 v[124:125], v[124:125], v[124:125], v[140:141]
	v_pk_add_f32 v[116:117], v[116:117], v[136:137]
	v_lshlrev_b32_e32 v128, 16, v80
	v_and_b32_e32 v129, 0xffff0000, v80
	v_lshlrev_b32_e32 v80, 16, v81
	v_and_b32_e32 v81, 0xffff0000, v81
	v_pk_mul_f32 v[142:143], v[78:79], v[78:79]
	v_pk_mul_f32 v[176:177], v[100:101], v[100:101]
	v_mul_f32_e32 v130, v153, v153
	v_mul_f32_e32 v138, v105, v105
	v_pk_add_f32 v[124:125], v[124:125], v[124:125] op_sel:[0,1] op_sel_hi:[1,0]
	v_pk_add_f32 v[116:117], v[116:117], v[116:117] op_sel:[0,1] op_sel_hi:[1,0]
	v_and_b32_e32 v133, 0xffff0000, v82
	v_lshlrev_b32_e32 v82, 16, v83
	v_and_b32_e32 v83, 0xffff0000, v83
	v_mul_f32_e32 v144, v129, v129
	v_mul_f32_e32 v146, v81, v81
	s_waitcnt vmcnt(4)
	v_lshlrev_b32_e32 v145, 16, v106
	v_and_b32_e32 v147, 0xffff0000, v106
	v_mov_b32_e32 v168, v126
	v_mov_b32_e32 v169, v78
	v_mov_b32_e32 v78, v127
	v_pk_fma_f32 v[126:127], v[126:127], v[126:127], v[142:143]
	v_mov_b32_e32 v188, v148
	v_mov_b32_e32 v189, v100
	v_mov_b32_e32 v100, v149
	v_pk_fma_f32 v[148:149], v[148:149], v[148:149], v[176:177]
	v_pk_fma_f32 v[170:171], v[152:153], v[152:153], v[130:131] op_sel_hi:[1,1,0]
	v_pk_fma_f32 v[176:177], v[104:105], v[104:105], v[138:139] op_sel_hi:[1,1,0]
	v_mov_b32_e32 v138, v124
	v_mov_b32_e32 v130, v116
	v_mul_f32_e32 v197, v133, v133
	v_mul_f32_e32 v198, v82, v82
	v_mul_f32_e32 v199, v83, v83
	v_pk_fma_f32 v[140:141], v[128:129], v[128:129], v[144:145] op_sel_hi:[1,1,0]
	v_pk_fma_f32 v[142:143], v[80:81], v[80:81], v[146:147] op_sel_hi:[1,1,0]
	v_pk_add_f32 v[126:127], v[126:127], v[126:127] op_sel:[0,1] op_sel_hi:[1,0]
	v_pk_add_f32 v[116:117], v[116:117], v[124:125]
	v_pk_mul_f32 v[124:125], v[130:131], v[138:139]
	v_mov_b32_e32 v141, v198
	v_mov_b32_e32 v143, v199
	v_mov_b32_e32 v127, v197
	v_mov_b32_e32 v117, v125
	v_pk_add_f32 v[140:141], v[140:141], v[142:143]
	v_pk_add_f32 v[116:117], v[116:117], v[126:127]
	v_lshlrev_b32_e32 v151, 16, v103
	v_lshlrev_b32_e32 v150, 16, v102
	v_and_b32_e32 v103, 0xffff0000, v103
	v_and_b32_e32 v102, 0xffff0000, v102
	s_waitcnt vmcnt(1)
; __device__ __forceinline__ float wave_sum(float v) {
; #pragma unroll
;     for (int o = 1; o < 64; o <<= 1) v += __shfl_xor(v, o);
;     return v;
; __global__ void __launch_bounds__(NTHREADS, 2) fwd(Args args) {
;     ...
;             for (int j = 0; j < 16; ++j) { const u32x2 q = xr[64 * j]; v[j] = (f32x4){bflo(q.x), bfhi(q.x), bflo(q.y), bfhi(q.y)}; ss += (v[j].x * v[j].x + v[j].y * v[j].y) + (v[j].z * v[j].z + v[j].w * v[j].w); }
;             const float rstd = 1.f / sqrtf(wave_sum(ss) * (1.f / D) + RMS_EPS);
	v_and_b32_e32 v159, 0xffff0000, v112
	v_pk_add_f32 v[116:117], v[116:117], v[140:141]
	v_lshlrev_b32_e32 v158, 16, v112
	v_pk_mul_f32 v[178:179], v[102:103], v[102:103]
	v_mul_f32_e32 v144, v159, v159
	v_pk_add_f32 v[142:143], v[148:149], v[148:149] op_sel:[0,1] op_sel_hi:[1,0]
	v_pk_add_f32 v[116:117], v[116:117], v[116:117] op_sel:[0,1] op_sel_hi:[1,0]
	v_lshlrev_b32_e32 v106, 16, v107
	v_and_b32_e32 v107, 0xffff0000, v107
	v_mov_b32_e32 v181, v145
	v_mov_b32_e32 v190, v150
	v_mov_b32_e32 v191, v102
	v_mov_b32_e32 v102, v151
	v_pk_fma_f32 v[150:151], v[150:151], v[150:151], v[178:179]
	v_pk_fma_f32 v[178:179], v[158:159], v[158:159], v[144:145] op_sel_hi:[1,1,0]
	v_mov_b32_e32 v180, v142
	v_mov_b32_e32 v144, v116
	v_mul_f32_e32 v200, v147, v147
	v_mul_f32_e32 v201, v106, v106
	v_mul_f32_e32 v202, v107, v107
	v_pk_add_f32 v[148:149], v[150:151], v[150:151] op_sel:[0,1] op_sel_hi:[1,0]
	v_pk_add_f32 v[116:117], v[116:117], v[142:143]
	v_pk_mul_f32 v[124:125], v[144:145], v[180:181]
	v_lshlrev_b32_e32 v155, 16, v109
	v_lshlrev_b32_e32 v154, 16, v108
	v_and_b32_e32 v109, 0xffff0000, v109
	v_and_b32_e32 v108, 0xffff0000, v108
	v_mov_b32_e32 v171, v201
	v_mov_b32_e32 v177, v202
	v_mov_b32_e32 v149, v200
	v_mov_b32_e32 v117, v125
	v_pk_mul_f32 v[182:183], v[108:109], v[108:109]
	v_pk_add_f32 v[120:121], v[170:171], v[176:177]
	v_pk_add_f32 v[116:117], v[116:117], v[148:149]
	v_lshlrev_b32_e32 v157, 16, v111
	v_lshlrev_b32_e32 v156, 16, v110
	v_and_b32_e32 v111, 0xffff0000, v111
	v_and_b32_e32 v110, 0xffff0000, v110
	v_lshlrev_b32_e32 v112, 16, v113
	v_and_b32_e32 v113, 0xffff0000, v113
	v_mov_b32_e32 v192, v154
	v_mov_b32_e32 v193, v108
	v_mov_b32_e32 v108, v155
	v_pk_fma_f32 v[154:155], v[154:155], v[154:155], v[182:183]
	v_pk_add_f32 v[116:117], v[116:117], v[120:121]
	s_waitcnt vmcnt(0)
	v_lshlrev_b32_e32 v161, 16, v114
	v_pk_mul_f32 v[184:185], v[110:111], v[110:111]
	v_mul_f32_e32 v160, v113, v113
	v_pk_add_f32 v[150:151], v[154:155], v[154:155] op_sel:[0,1] op_sel_hi:[1,0]
	v_pk_add_f32 v[116:117], v[116:117], v[116:117] op_sel:[0,1] op_sel_hi:[1,0]
	v_and_b32_e32 v163, 0xffff0000, v114
	v_lshlrev_b32_e32 v114, 16, v115
	v_and_b32_e32 v115, 0xffff0000, v115
	v_mov_b32_e32 v187, v161
	v_mov_b32_e32 v194, v156
	v_mov_b32_e32 v195, v110
	v_mov_b32_e32 v110, v157
	v_pk_fma_f32 v[156:157], v[156:157], v[156:157], v[184:185]
	v_pk_fma_f32 v[182:183], v[112:113], v[112:113], v[160:161] op_sel_hi:[1,1,0]
	v_mov_b32_e32 v186, v150
	v_mov_b32_e32 v160, v116
	v_mul_f32_e32 v203, v163, v163
	v_mul_f32_e32 v204, v114, v114
	v_mul_f32_e32 v205, v115, v115
	v_pk_add_f32 v[154:155], v[156:157], v[156:157] op_sel:[0,1] op_sel_hi:[1,0]
	v_pk_add_f32 v[116:117], v[116:117], v[150:151]
	v_pk_mul_f32 v[120:121], v[160:161], v[186:187]
	v_mov_b32_e32 v179, v204
	v_mov_b32_e32 v183, v205
	v_mov_b32_e32 v155, v203
	v_mov_b32_e32 v117, v121
	v_pk_add_f32 v[156:157], v[178:179], v[182:183]
	v_pk_add_f32 v[116:117], v[116:117], v[154:155]
	v_addc_co_u32_e32 v91, vcc, 0, v67, vcc
	v_pk_add_f32 v[116:117], v[116:117], v[156:157]
	v_mov_b32_e32 v132, v131
	v_add_f32_e32 v116, v116, v117
	ds_bpermute_b32 v117, v92, v116
	v_mov_b32_e32 v146, v145
	v_mov_b32_e32 v162, v161
	s_waitcnt lgkmcnt(0)
	v_add_f32_e32 v116, v116, v117
	ds_bpermute_b32 v117, v93, v116
	s_waitcnt lgkmcnt(0)
	v_add_f32_e32 v116, v116, v117
	ds_bpermute_b32 v117, v94, v116
	s_waitcnt lgkmcnt(0)
	v_add_f32_e32 v116, v116, v117
	ds_bpermute_b32 v117, v95, v116
	s_waitcnt lgkmcnt(0)
	v_add_f32_e32 v116, v116, v117
	ds_bpermute_b32 v117, v96, v116
	s_waitcnt lgkmcnt(0)
	v_add_f32_e32 v116, v116, v117
	ds_bpermute_b32 v117, v97, v116
	s_waitcnt lgkmcnt(0)
; __global__ void __launch_bounds__(NTHREADS, 2) fwd(Args args) {
;     ...
;             const float rstd = 1.f / sqrtf(wave_sum(ss) * (1.f / D) + RMS_EPS);
;             f32x4* orow = (f32x4*)(args.out + (size_t)m * D) + F.lane;
; #pragma unroll
;             for (int j = 0; j < 16; ++j) orow[64 * j] = v[j] * rstd * gv[j]; } }
	v_add_f32_e32 v116, v116, v117
	v_fmamk_f32 v116, v116, 0x39800000, v98
	v_mul_f32_e32 v117, 0x4f800000, v116
	v_cmp_gt_f32_e32 vcc, s3, v116
	s_nop 1
	v_cndmask_b32_e32 v116, v116, v117, vcc
	v_sqrt_f32_e32 v117, v116
	s_nop 0
	v_add_u32_e32 v120, -1, v117
	v_add_u32_e32 v121, 1, v117
	v_fma_f32 v124, -v120, v117, v116
	v_fma_f32 v125, -v121, v117, v116
	v_cmp_ge_f32_e64 s[0:1], 0, v124
	s_nop 1
	v_cndmask_b32_e64 v117, v117, v120, s[0:1]
	v_cmp_lt_f32_e64 s[0:1], 0, v125
	s_nop 1
	v_cndmask_b32_e64 v117, v117, v121, s[0:1]
	v_mul_f32_e32 v120, 0x37800000, v117
	v_cndmask_b32_e32 v117, v117, v120, vcc
	v_cmp_class_f32_e32 vcc, v116, v99
	s_nop 1
	v_cndmask_b32_e32 v116, v117, v116, vcc
	v_div_scale_f32 v117, s[0:1], v116, v116, 1.0
	v_rcp_f32_e32 v121, v117
	v_div_scale_f32 v120, vcc, 1.0, v116, 1.0
	v_fma_f32 v124, -v117, v121, 1.0
	v_fmac_f32_e32 v121, v124, v121
	v_mul_f32_e32 v124, v120, v121
	v_fma_f32 v125, -v117, v124, v120
	v_fmac_f32_e32 v124, v125, v121
	v_fma_f32 v117, -v117, v124, v120
	v_div_fmas_f32 v117, v117, v121, v124
	v_div_fixup_f32 v116, v117, v116, 1.0
	v_pk_mul_f32 v[88:89], v[116:117], v[88:89] op_sel_hi:[0,1]
	v_pk_mul_f32 v[68:69], v[116:117], v[68:69] op_sel_hi:[0,1]
	v_pk_mul_f32 v[120:121], v[116:117], v[164:165] op_sel_hi:[0,1]
	v_pk_mul_f32 v[124:125], v[116:117], v[70:71] op_sel_hi:[0,1]
	v_pk_mul_f32 v[118:119], v[116:117], v[118:119] op_sel_hi:[0,1]
	v_pk_mul_f32 v[126:127], v[116:117], v[72:73] op_sel_hi:[0,1]
	v_pk_mul_f32 v[122:123], v[116:117], v[122:123] op_sel_hi:[0,1]
	v_pk_mul_f32 v[130:131], v[116:117], v[74:75] op_sel_hi:[0,1]
	v_pk_mul_f32 v[134:135], v[116:117], v[166:167] op_sel_hi:[0,1]
	v_pk_mul_f32 v[136:137], v[116:117], v[76:77] op_sel_hi:[0,1]
	v_pk_mul_f32 v[138:139], v[116:117], v[168:169] op_sel_hi:[0,1]
	v_pk_mul_f32 v[140:141], v[116:117], v[78:79] op_sel_hi:[0,1]
	v_pk_mul_f32 v[128:129], v[116:117], v[128:129] op_sel_hi:[0,1]
	v_pk_mul_f32 v[142:143], v[116:117], v[80:81] op_sel_hi:[0,1]
	v_pk_mul_f32 v[132:133], v[116:117], v[132:133] op_sel_hi:[0,1]
	v_pk_mul_f32 v[144:145], v[116:117], v[82:83] op_sel_hi:[0,1]
	v_pk_mul_f32 v[148:149], v[116:117], v[188:189] op_sel_hi:[0,1]
	v_pk_mul_f32 v[150:151], v[116:117], v[100:101] op_sel_hi:[0,1]
	v_pk_mul_f32 v[154:155], v[116:117], v[190:191] op_sel_hi:[0,1]
	v_pk_mul_f32 v[156:157], v[116:117], v[102:103] op_sel_hi:[0,1]
	v_pk_mul_f32 v[152:153], v[116:117], v[152:153] op_sel_hi:[0,1]
	v_pk_mul_f32 v[160:161], v[116:117], v[104:105] op_sel_hi:[0,1]
	v_pk_mul_f32 v[146:147], v[116:117], v[146:147] op_sel_hi:[0,1]
	v_pk_mul_f32 v[164:165], v[116:117], v[106:107] op_sel_hi:[0,1]
	v_pk_mul_f32 v[166:167], v[116:117], v[192:193] op_sel_hi:[0,1]
	v_pk_mul_f32 v[168:169], v[116:117], v[108:109] op_sel_hi:[0,1]
	v_pk_mul_f32 v[170:171], v[116:117], v[194:195] op_sel_hi:[0,1]
	v_pk_mul_f32 v[172:173], v[116:117], v[110:111] op_sel_hi:[0,1]
	v_pk_mul_f32 v[158:159], v[116:117], v[158:159] op_sel_hi:[0,1]
	v_pk_mul_f32 v[174:175], v[116:117], v[112:113] op_sel_hi:[0,1]
	v_pk_mul_f32 v[162:163], v[116:117], v[162:163] op_sel_hi:[0,1]
	v_pk_mul_f32 v[176:177], v[116:117], v[114:115] op_sel_hi:[0,1]
	v_pk_mul_f32 v[70:71], v[68:69], v[2:3]
	v_pk_mul_f32 v[68:69], v[88:89], v[0:1]
	v_pk_mul_f32 v[74:75], v[124:125], v[6:7]
	v_pk_mul_f32 v[72:73], v[120:121], v[4:5]
	v_pk_mul_f32 v[78:79], v[126:127], v[10:11]
	v_pk_mul_f32 v[76:77], v[118:119], v[8:9]
	v_pk_mul_f32 v[82:83], v[130:131], v[14:15]
	v_pk_mul_f32 v[80:81], v[122:123], v[12:13]
	v_pk_mul_f32 v[102:103], v[136:137], v[18:19]
	v_pk_mul_f32 v[100:101], v[134:135], v[16:17]
	v_pk_mul_f32 v[106:107], v[140:141], v[22:23]
	v_pk_mul_f32 v[104:105], v[138:139], v[20:21]
	v_pk_mul_f32 v[110:111], v[142:143], v[26:27]
	v_pk_mul_f32 v[108:109], v[128:129], v[24:25]
	v_pk_mul_f32 v[114:115], v[144:145], v[30:31]
	v_pk_mul_f32 v[112:113], v[132:133], v[28:29]
	v_pk_mul_f32 v[118:119], v[150:151], v[34:35]
	v_pk_mul_f32 v[116:117], v[148:149], v[32:33]
	v_pk_mul_f32 v[122:123], v[156:157], v[38:39]
	v_pk_mul_f32 v[120:121], v[154:155], v[36:37]
	v_pk_mul_f32 v[126:127], v[160:161], v[42:43]
	v_pk_mul_f32 v[124:125], v[152:153], v[40:41]
	v_pk_mul_f32 v[130:131], v[164:165], v[46:47]
	v_pk_mul_f32 v[128:129], v[146:147], v[44:45]
	v_pk_mul_f32 v[134:135], v[168:169], v[50:51]
	v_pk_mul_f32 v[132:133], v[166:167], v[48:49]
	v_pk_mul_f32 v[138:139], v[172:173], v[54:55]
	v_pk_mul_f32 v[136:137], v[170:171], v[52:53]
	v_pk_mul_f32 v[142:143], v[174:175], v[58:59]
	v_pk_mul_f32 v[140:141], v[158:159], v[56:57]
	v_pk_mul_f32 v[146:147], v[176:177], v[62:63]
	v_pk_mul_f32 v[144:145], v[162:163], v[60:61]
	global_store_dwordx4 v[66:67], v[68:71], off nt
	global_store_dwordx4 v[66:67], v[72:75], off offset:1024 nt
	global_store_dwordx4 v[66:67], v[76:79], off offset:2048 nt
	global_store_dwordx4 v[66:67], v[80:83], off offset:3072 nt
	global_store_dwordx4 v[86:87], v[100:103], off offset:-4096 nt
	global_store_dwordx4 v[84:85], v[104:107], off offset:1024 nt
	global_store_dwordx4 v[84:85], v[108:111], off offset:2048 nt
	global_store_dwordx4 v[84:85], v[112:115], off offset:3072 nt
	global_store_dwordx4 v[86:87], v[116:119], off nt
	global_store_dwordx4 v[86:87], v[120:123], off offset:1024 nt
	global_store_dwordx4 v[86:87], v[124:127], off offset:2048 nt
	global_store_dwordx4 v[86:87], v[128:131], off offset:3072 nt
	global_store_dwordx4 v[90:91], v[132:135], off nt
	global_store_dwordx4 v[90:91], v[136:139], off offset:1024 nt
	global_store_dwordx4 v[90:91], v[140:143], off offset:2048 nt
	global_store_dwordx4 v[90:91], v[144:147], off offset:3072 nt
	v_lshl_add_u64 v[66:67], v[66:67], 0, s[6:7]
	s_cbranch_scc1 .LBB0_1794
